# P7 side-job fast path trimmed: linear job addresses (c<<12, c<<14) with SADDR store/loads, 8 v_mul_f32 instead of 4 v_pk_mul_f32; 52 -> 39 instructions per job
# baseline (speedup 1.0000x reference)
; #define PG8_LAS __attribute__((address_space(3)))
;     __device__ __forceinline__ void issue(PG8_LAS unsigned char* lds0, int j, int tid, int wid) const {
;         const float* s0; unsigned char* d; addr(j, tid, s0, d);
;         __builtin_amdgcn_global_load_lds((const unsigned*)s0, (PG8_LAS unsigned*)(lds0 + stage + wid * 1024), 16, 0, 2);
;         __builtin_amdgcn_global_load_lds((const unsigned*)(s0 + ntot), (PG8_LAS unsigned*)(lds0 + stage + 8192 + wid * 1024), 16, 0, 2);
;     }
;     __device__ __forceinline__ void read(v4i_t& t0, v4i_t& t1, int tid, unsigned ldsb) const {
;         asm volatile("ds_read_b128 %0, %1" : "=&v"(t0) : "v"(ldsb + stage + 16u * (unsigned)tid) : "memory");
;         asm volatile("ds_read_b128 %0, %1" : "=&v"(t1) : "v"(ldsb + stage + 8192u + 16u * (unsigned)tid) : "memory");
;     }
;     __device__ __forceinline__ void finish(v4i_t& t0, v4i_t& t1, int j, int tid) const {
;         asm volatile("" : "+v"(t0), "+v"(t1));
;         const float* s0; unsigned char* d; addr(j, tid, s0, d);
;         const f32x4 r0 = __builtin_bit_cast(f32x4, t0) * 64.f, r1 = __builtin_bit_cast(f32x4, t1) * 64.f;
;         int w0 = 0, w1 = 0; w0 = __builtin_amdgcn_cvt_pk_fp8_f32(r0[0], r1[0], w0, false); w0 = __builtin_amdgcn_cvt_pk_fp8_f32(r0[1], r1[1], w0, true);
;         w1 = __builtin_amdgcn_cvt_pk_fp8_f32(r0[2], r1[2], w1, false); w1 = __builtin_amdgcn_cvt_pk_fp8_f32(r0[3], r1[3], w1, true);
;         typedef int v2is __attribute__((ext_vector_type(2))); __builtin_nontemporal_store((v2is){w0, w1}, (v2is*)d);
.Lp7vg_wd_a1:
	s_waitcnt lgkmcnt(0)
	s_barrier
	s_cmp_lt_i32 s98, 0
	s_cbranch_scc1 .Lp7vg_mmslow_a
	s_cmpk_gt_i32 s48, 0x7f
	s_cbranch_scc1 .Lp7vg_mmslow_a
	s_setprio 1
	s_waitcnt lgkmcnt(0)
	v_mfma_scale_f32_16x16x128_f8f6f4 v[202:205], v[26:33], v[58:65], v[202:205], v226, v226 op_sel_hi:[0,0,0]
	s_add_i32 s4, s98, s52
	s_add_i32 s4, s4, 1
	v_mul_f32_e32 v70, s14, v70
	v_mfma_scale_f32_16x16x128_f8f6f4 v[198:201], v[18:25], v[58:65], v[198:201], v226, v226 op_sel_hi:[0,0,0]
	v_mul_f32_e32 v74, s14, v74
	v_mul_f32_e32 v71, s14, v71
	v_mul_f32_e32 v75, s14, v75
	v_mfma_scale_f32_16x16x128_f8f6f4 v[186:189], v[26:33], v[50:57], v[186:189], v226, v226 op_sel_hi:[0,0,0]
	s_lshl_b32 s4, s4, 12
	v_cvt_pk_fp8_f32 v70, v70, v74
	v_mul_f32_e32 v72, s14, v72
	v_mfma_scale_f32_16x16x128_f8f6f4 v[182:185], v[18:25], v[50:57], v[182:185], v226, v226 op_sel_hi:[0,0,0]
	v_mul_f32_e32 v76, s14, v76
	v_cvt_pk_fp8_f32 v70, v71, v75 op_sel:[0,0,1]
	v_mul_f32_e32 v73, s14, v73
	v_mfma_scale_f32_16x16x128_f8f6f4 v[170:173], v[26:33], v[42:49], v[170:173], v226, v226 op_sel_hi:[0,0,0]
	v_mul_f32_e32 v77, s14, v77
	v_readlane_b32 s2, v251, 50
	v_cvt_pk_fp8_f32 v71, v72, v76
	v_mfma_scale_f32_16x16x128_f8f6f4 v[166:169], v[18:25], v[42:49], v[166:169], v226, v226 op_sel_hi:[0,0,0]
	v_readlane_b32 s3, v251, 51
	v_cvt_pk_fp8_f32 v71, v73, v77 op_sel:[0,0,1]
	s_add_u32 s2, s2, s4
	s_addc_u32 s3, s3, 0
	v_mfma_scale_f32_16x16x128_f8f6f4 v[154:157], v[26:33], v[34:41], v[154:157], v226, v226 op_sel_hi:[0,0,0]
	global_store_dwordx2 v210, v[70:71], s[2:3] nt
	s_add_i32 s4, s48, s53
	s_lshl_b32 s4, s4, 14
	v_mfma_scale_f32_16x16x128_f8f6f4 v[150:153], v[18:25], v[34:41], v[150:153], v226, v226 op_sel_hi:[0,0,0]
	s_setprio 0
	s_setprio 1
	s_add_u32 s2, s76, s4
	s_addc_u32 s3, s77, 0
	s_add_u32 s4, s2, s16
	s_addc_u32 s5, s3, s17
	v_mfma_scale_f32_16x16x128_f8f6f4 v[194:197], v[10:17], v[58:65], v[194:197], v226, v226 op_sel_hi:[0,0,0]
	v_lshlrev_b32_e32 v66, 2, v208
	global_load_dwordx4 v[70:73], v66, s[2:3] nt
	global_load_dwordx4 v[74:77], v66, s[4:5] nt
	v_mfma_scale_f32_16x16x128_f8f6f4 v[190:193], v[2:9], v[58:65], v[190:193], v226, v226 op_sel_hi:[0,0,0]
	s_mov_b32 s100, 3
	s_mov_b32 s98, s48
	s_add_i32 s48, s48, 1
	v_mfma_scale_f32_16x16x128_f8f6f4 v[178:181], v[10:17], v[50:57], v[178:181], v226, v226 op_sel_hi:[0,0,0]
	s_add_u32 s2, s42, 0xfffc0080
	s_addc_u32 s3, s43, -1
	s_cmp_eq_u32 s64, 12
	s_cselect_b32 s5, s23, s3
	s_cselect_b32 s4, s25, s2
	s_cselect_b32 s45, s35, s63
	s_cselect_b32 s44, s61, s62
	v_mfma_scale_f32_16x16x128_f8f6f4 v[174:177], v[2:9], v[50:57], v[174:177], v226, v226 op_sel_hi:[0,0,0]
	v_mfma_scale_f32_16x16x128_f8f6f4 v[162:165], v[10:17], v[42:49], v[162:165], v226, v226 op_sel_hi:[0,0,0]
	v_mfma_scale_f32_16x16x128_f8f6f4 v[158:161], v[2:9], v[42:49], v[158:161], v226, v226 op_sel_hi:[0,0,0]
	v_mfma_scale_f32_16x16x128_f8f6f4 v[146:149], v[10:17], v[34:41], v[146:149], v226, v226 op_sel_hi:[0,0,0]
	v_mfma_scale_f32_16x16x128_f8f6f4 v[142:145], v[2:9], v[34:41], v[142:145], v226, v226 op_sel_hi:[0,0,0]
	s_setprio 0
	s_branch .Lp7vg_mmjoin_a

; #define PG8_LAS __attribute__((address_space(3)))
;     __device__ __forceinline__ void issue(PG8_LAS unsigned char* lds0, int j, int tid, int wid) const {
;         const float* s0; unsigned char* d; addr(j, tid, s0, d);
;         __builtin_amdgcn_global_load_lds((const unsigned*)s0, (PG8_LAS unsigned*)(lds0 + stage + wid * 1024), 16, 0, 2);
;         __builtin_amdgcn_global_load_lds((const unsigned*)(s0 + ntot), (PG8_LAS unsigned*)(lds0 + stage + 8192 + wid * 1024), 16, 0, 2);
;     }
;     __device__ __forceinline__ void read(v4i_t& t0, v4i_t& t1, int tid, unsigned ldsb) const {
;         asm volatile("ds_read_b128 %0, %1" : "=&v"(t0) : "v"(ldsb + stage + 16u * (unsigned)tid) : "memory");
;         asm volatile("ds_read_b128 %0, %1" : "=&v"(t1) : "v"(ldsb + stage + 8192u + 16u * (unsigned)tid) : "memory");
;     }
;     __device__ __forceinline__ void finish(v4i_t& t0, v4i_t& t1, int j, int tid) const {
;         asm volatile("" : "+v"(t0), "+v"(t1));
;         const float* s0; unsigned char* d; addr(j, tid, s0, d);
;         const f32x4 r0 = __builtin_bit_cast(f32x4, t0) * 64.f, r1 = __builtin_bit_cast(f32x4, t1) * 64.f;
;         int w0 = 0, w1 = 0; w0 = __builtin_amdgcn_cvt_pk_fp8_f32(r0[0], r1[0], w0, false); w0 = __builtin_amdgcn_cvt_pk_fp8_f32(r0[1], r1[1], w0, true);
;         w1 = __builtin_amdgcn_cvt_pk_fp8_f32(r0[2], r1[2], w1, false); w1 = __builtin_amdgcn_cvt_pk_fp8_f32(r0[3], r1[3], w1, true);
;         typedef int v2is __attribute__((ext_vector_type(2))); __builtin_nontemporal_store((v2is){w0, w1}, (v2is*)d);
.Lp7vg_wd_b1:
	s_waitcnt lgkmcnt(0)
	s_barrier
	s_cmp_lt_i32 s99, 0
	s_cbranch_scc1 .Lp7vg_mmslow_b
	s_cmpk_gt_i32 s48, 0x7f
	s_cbranch_scc1 .Lp7vg_mmslow_b
	s_setprio 1
	s_waitcnt lgkmcnt(0)
	v_mfma_scale_f32_16x16x128_f8f6f4 v[202:205], v[26:33], v[58:65], v[202:205], v226, v226 op_sel_hi:[0,0,0]
	s_add_i32 s65, s99, s52
	s_add_i32 s65, s65, 1
	v_mul_f32_e32 v242, s14, v242
	v_mfma_scale_f32_16x16x128_f8f6f4 v[198:201], v[18:25], v[58:65], v[198:201], v226, v226 op_sel_hi:[0,0,0]
	v_mul_f32_e32 v246, s14, v246
	v_mul_f32_e32 v243, s14, v243
	v_mul_f32_e32 v247, s14, v247
	v_mfma_scale_f32_16x16x128_f8f6f4 v[186:189], v[26:33], v[50:57], v[186:189], v226, v226 op_sel_hi:[0,0,0]
	s_lshl_b32 s65, s65, 12
	v_cvt_pk_fp8_f32 v242, v242, v246
	v_mul_f32_e32 v244, s14, v244
	v_mfma_scale_f32_16x16x128_f8f6f4 v[182:185], v[18:25], v[50:57], v[182:185], v226, v226 op_sel_hi:[0,0,0]
	v_mul_f32_e32 v248, s14, v248
	v_cvt_pk_fp8_f32 v242, v243, v247 op_sel:[0,0,1]
	v_mul_f32_e32 v245, s14, v245
	v_mfma_scale_f32_16x16x128_f8f6f4 v[170:173], v[26:33], v[42:49], v[170:173], v226, v226 op_sel_hi:[0,0,0]
	v_mul_f32_e32 v249, s14, v249
	v_readlane_b32 s46, v251, 50
	v_cvt_pk_fp8_f32 v243, v244, v248
	v_mfma_scale_f32_16x16x128_f8f6f4 v[166:169], v[18:25], v[42:49], v[166:169], v226, v226 op_sel_hi:[0,0,0]
	v_readlane_b32 s47, v251, 51
	v_cvt_pk_fp8_f32 v243, v245, v249 op_sel:[0,0,1]
	s_add_u32 s46, s46, s65
	s_addc_u32 s47, s47, 0
	v_mfma_scale_f32_16x16x128_f8f6f4 v[154:157], v[26:33], v[34:41], v[154:157], v226, v226 op_sel_hi:[0,0,0]
	global_store_dwordx2 v210, v[242:243], s[46:47] nt
	s_add_i32 s65, s48, s53
	s_lshl_b32 s65, s65, 14
	v_mfma_scale_f32_16x16x128_f8f6f4 v[150:153], v[18:25], v[34:41], v[150:153], v226, v226 op_sel_hi:[0,0,0]
	s_setprio 0
	s_setprio 1
	s_add_u32 s46, s76, s65
	s_addc_u32 s47, s77, 0
	s_add_u32 s4, s46, s16
	s_addc_u32 s5, s47, s17
	v_mfma_scale_f32_16x16x128_f8f6f4 v[194:197], v[10:17], v[58:65], v[194:197], v226, v226 op_sel_hi:[0,0,0]
	v_lshlrev_b32_e32 v66, 2, v208
	global_load_dwordx4 v[242:245], v66, s[46:47] nt
	global_load_dwordx4 v[246:249], v66, s[4:5] nt
	v_mfma_scale_f32_16x16x128_f8f6f4 v[190:193], v[2:9], v[58:65], v[190:193], v226, v226 op_sel_hi:[0,0,0]
	s_mov_b32 s100, 3
	s_mov_b32 s99, s48
	s_add_i32 s48, s48, 1
	v_mfma_scale_f32_16x16x128_f8f6f4 v[178:181], v[10:17], v[50:57], v[178:181], v226, v226 op_sel_hi:[0,0,0]
	s_add_u32 s46, s44, 0x84000
	s_addc_u32 s47, s45, 0
	v_mfma_scale_f32_16x16x128_f8f6f4 v[174:177], v[2:9], v[50:57], v[174:177], v226, v226 op_sel_hi:[0,0,0]
	v_mfma_scale_f32_16x16x128_f8f6f4 v[162:165], v[10:17], v[42:49], v[162:165], v226, v226 op_sel_hi:[0,0,0]
	v_mfma_scale_f32_16x16x128_f8f6f4 v[158:161], v[2:9], v[42:49], v[158:161], v226, v226 op_sel_hi:[0,0,0]
	v_mfma_scale_f32_16x16x128_f8f6f4 v[146:149], v[10:17], v[34:41], v[146:149], v226, v226 op_sel_hi:[0,0,0]
	v_mfma_scale_f32_16x16x128_f8f6f4 v[142:145], v[2:9], v[34:41], v[142:145], v226, v226 op_sel_hi:[0,0,0]
	s_setprio 0
	s_branch .Lp7vg_mmjoin_b
